# the three GEMM K loop heads placed on 64-byte boundaries (on top of v21)
# baseline (speedup 1.0000x reference)
.LBB0_300:
	s_ashr_i32 s59, s58, 31
	s_lshl_b64 s[60:61], s[58:59], 20
	s_add_u32 s60, s3, s60
	s_addc_u32 s61, s72, s61
	s_and_b64 s[62:63], s[8:9], exec
	s_cselect_b32 s11, s61, s67
	s_cselect_b32 s16, s60, s66
	s_ashr_i32 s57, s56, 31
	s_lshl_b64 s[62:63], s[56:57], 20
	s_add_u32 s62, s73, s62
	s_addc_u32 s63, s74, s63
	s_and_b64 s[70:71], s[8:9], exec
	s_cselect_b32 s57, s63, s69
	s_cselect_b32 s59, s62, s68
	s_add_u32 s66, s66, 0x80080
	s_addc_u32 s67, s67, 0
	s_add_u32 s92, s68, 0x100
	v_mov_b32_e32 v2, 0
	s_addc_u32 s93, s69, 0
	s_mov_b32 s94, -2
	v_mov_b32_e32 v3, v2
	v_mov_b32_e32 v4, v2
	v_mov_b32_e32 v5, v2
	v_mov_b32_e32 v6, v2
	v_mov_b32_e32 v7, v2
	v_mov_b32_e32 v8, v2
	v_mov_b32_e32 v9, v2
	v_mov_b32_e32 v18, v2
	v_mov_b32_e32 v19, v2
	v_mov_b32_e32 v20, v2
	v_mov_b32_e32 v21, v2
	v_mov_b32_e32 v22, v2
	v_mov_b32_e32 v23, v2
	v_mov_b32_e32 v24, v2
	v_mov_b32_e32 v25, v2
	v_mov_b32_e32 v34, v2
	v_mov_b32_e32 v35, v2
	v_mov_b32_e32 v36, v2
	v_mov_b32_e32 v37, v2
	v_mov_b32_e32 v38, v2
	v_mov_b32_e32 v39, v2
	v_mov_b32_e32 v40, v2
	v_mov_b32_e32 v41, v2
	v_mov_b32_e32 v50, v2
	v_mov_b32_e32 v51, v2
	v_mov_b32_e32 v52, v2
	v_mov_b32_e32 v53, v2
	v_mov_b32_e32 v54, v2
	v_mov_b32_e32 v55, v2
	v_mov_b32_e32 v56, v2
	v_mov_b32_e32 v57, v2
	v_mov_b32_e32 v10, v2
	v_mov_b32_e32 v11, v2
	v_mov_b32_e32 v12, v2
	v_mov_b32_e32 v13, v2
	v_mov_b32_e32 v14, v2
	v_mov_b32_e32 v15, v2
	v_mov_b32_e32 v16, v2
	v_mov_b32_e32 v17, v2
	v_mov_b32_e32 v26, v2
	v_mov_b32_e32 v27, v2
	v_mov_b32_e32 v28, v2
	v_mov_b32_e32 v29, v2
	v_mov_b32_e32 v30, v2
	v_mov_b32_e32 v31, v2
	v_mov_b32_e32 v32, v2
	v_mov_b32_e32 v33, v2
	v_mov_b32_e32 v42, v2
	v_mov_b32_e32 v43, v2
	v_mov_b32_e32 v44, v2
	v_mov_b32_e32 v45, v2
	v_mov_b32_e32 v46, v2
	v_mov_b32_e32 v47, v2
	v_mov_b32_e32 v48, v2
	v_mov_b32_e32 v49, v2
	v_mov_b32_e32 v58, v2
	v_mov_b32_e32 v59, v2
	v_mov_b32_e32 v60, v2
	v_mov_b32_e32 v61, v2
	v_mov_b32_e32 v62, v2
	v_mov_b32_e32 v63, v2
	v_mov_b32_e32 v64, v2
	v_mov_b32_e32 v65, v2
	v_mov_b32_e32 v66, v2
	v_mov_b32_e32 v67, v2
	v_mov_b32_e32 v68, v2
	v_mov_b32_e32 v69, v2
	v_mov_b32_e32 v70, v2
	v_mov_b32_e32 v71, v2
	v_mov_b32_e32 v72, v2
	v_mov_b32_e32 v73, v2
	v_mov_b32_e32 v82, v2
	v_mov_b32_e32 v83, v2
	v_mov_b32_e32 v84, v2
	v_mov_b32_e32 v85, v2
	v_mov_b32_e32 v86, v2
	v_mov_b32_e32 v87, v2
	v_mov_b32_e32 v88, v2
	v_mov_b32_e32 v89, v2
	v_mov_b32_e32 v98, v2
	v_mov_b32_e32 v99, v2
	v_mov_b32_e32 v100, v2
	v_mov_b32_e32 v101, v2
	v_mov_b32_e32 v102, v2
	v_mov_b32_e32 v103, v2
	v_mov_b32_e32 v104, v2
	v_mov_b32_e32 v105, v2
	v_mov_b32_e32 v122, v2
	v_mov_b32_e32 v123, v2
	v_mov_b32_e32 v124, v2
	v_mov_b32_e32 v125, v2
	v_mov_b32_e32 v134, v2
	v_mov_b32_e32 v135, v2
	v_mov_b32_e32 v136, v2
	v_mov_b32_e32 v137, v2
	v_mov_b32_e32 v74, v2
	v_mov_b32_e32 v75, v2
	v_mov_b32_e32 v76, v2
	v_mov_b32_e32 v77, v2
	v_mov_b32_e32 v78, v2
	v_mov_b32_e32 v79, v2
	v_mov_b32_e32 v80, v2
	v_mov_b32_e32 v81, v2
	v_mov_b32_e32 v90, v2
	v_mov_b32_e32 v91, v2
	v_mov_b32_e32 v92, v2
	v_mov_b32_e32 v93, v2
	v_mov_b32_e32 v94, v2
	v_mov_b32_e32 v95, v2
	v_mov_b32_e32 v96, v2
	v_mov_b32_e32 v97, v2
	v_mov_b32_e32 v114, v2
	v_mov_b32_e32 v115, v2
	v_mov_b32_e32 v116, v2
	v_mov_b32_e32 v117, v2
	v_mov_b32_e32 v118, v2
	v_mov_b32_e32 v119, v2
	v_mov_b32_e32 v120, v2
	v_mov_b32_e32 v121, v2
	v_mov_b32_e32 v138, v2
	v_mov_b32_e32 v139, v2
	v_mov_b32_e32 v140, v2
	v_mov_b32_e32 v141, v2
	v_mov_b32_e32 v142, v2
	v_mov_b32_e32 v143, v2
	v_mov_b32_e32 v144, v2
	v_mov_b32_e32 v145, v2
	.p2align 6

.LBB0_1598:
	s_ashr_i32 s41, s40, 31
	s_lshl_b64 s[42:43], s[40:41], 20
	s_add_u32 s42, s60, s42
	s_addc_u32 s43, s61, s43
	s_and_b64 s[50:51], s[8:9], exec
	s_cselect_b32 s41, s43, s55
	s_cselect_b32 s78, s42, s54
	s_ashr_i32 s39, s38, 31
	s_lshl_b64 s[50:51], s[38:39], 20
	s_add_u32 s50, s62, s50
	s_addc_u32 s51, s63, s51
	s_and_b64 s[58:59], s[8:9], exec
	s_cselect_b32 s39, s51, s57
	s_cselect_b32 s79, s50, s56
	s_add_u32 s54, s54, 0x80080
	s_addc_u32 s55, s55, 0
	s_add_u32 s80, s56, 0x100
	v_mov_b32_e32 v2, 0
	s_addc_u32 s81, s57, 0
	s_mov_b32 s82, -2
	v_mov_b32_e32 v3, v2
	v_mov_b32_e32 v4, v2
	v_mov_b32_e32 v5, v2
	v_mov_b32_e32 v6, v2
	v_mov_b32_e32 v7, v2
	v_mov_b32_e32 v8, v2
	v_mov_b32_e32 v9, v2
	v_mov_b32_e32 v18, v2
	v_mov_b32_e32 v19, v2
	v_mov_b32_e32 v20, v2
	v_mov_b32_e32 v21, v2
	v_mov_b32_e32 v22, v2
	v_mov_b32_e32 v23, v2
	v_mov_b32_e32 v24, v2
	v_mov_b32_e32 v25, v2
	v_mov_b32_e32 v34, v2
	v_mov_b32_e32 v35, v2
	v_mov_b32_e32 v36, v2
	v_mov_b32_e32 v37, v2
	v_mov_b32_e32 v38, v2
	v_mov_b32_e32 v39, v2
	v_mov_b32_e32 v40, v2
	v_mov_b32_e32 v41, v2
	v_mov_b32_e32 v50, v2
	v_mov_b32_e32 v51, v2
	v_mov_b32_e32 v52, v2
	v_mov_b32_e32 v53, v2
	v_mov_b32_e32 v54, v2
	v_mov_b32_e32 v55, v2
	v_mov_b32_e32 v56, v2
	v_mov_b32_e32 v57, v2
	v_mov_b32_e32 v10, v2
	v_mov_b32_e32 v11, v2
	v_mov_b32_e32 v12, v2
	v_mov_b32_e32 v13, v2
	v_mov_b32_e32 v14, v2
	v_mov_b32_e32 v15, v2
	v_mov_b32_e32 v16, v2
	v_mov_b32_e32 v17, v2
	v_mov_b32_e32 v26, v2
	v_mov_b32_e32 v27, v2
	v_mov_b32_e32 v28, v2
	v_mov_b32_e32 v29, v2
	v_mov_b32_e32 v30, v2
	v_mov_b32_e32 v31, v2
	v_mov_b32_e32 v32, v2
	v_mov_b32_e32 v33, v2
	v_mov_b32_e32 v42, v2
	v_mov_b32_e32 v43, v2
	v_mov_b32_e32 v44, v2
	v_mov_b32_e32 v45, v2
	v_mov_b32_e32 v46, v2
	v_mov_b32_e32 v47, v2
	v_mov_b32_e32 v48, v2
	v_mov_b32_e32 v49, v2
	v_mov_b32_e32 v58, v2
	v_mov_b32_e32 v59, v2
	v_mov_b32_e32 v60, v2
	v_mov_b32_e32 v61, v2
	v_mov_b32_e32 v62, v2
	v_mov_b32_e32 v63, v2
	v_mov_b32_e32 v64, v2
	v_mov_b32_e32 v65, v2
	v_mov_b32_e32 v66, v2
	v_mov_b32_e32 v67, v2
	v_mov_b32_e32 v68, v2
	v_mov_b32_e32 v69, v2
	v_mov_b32_e32 v70, v2
	v_mov_b32_e32 v71, v2
	v_mov_b32_e32 v72, v2
	v_mov_b32_e32 v73, v2
	v_mov_b32_e32 v82, v2
	v_mov_b32_e32 v83, v2
	v_mov_b32_e32 v84, v2
	v_mov_b32_e32 v85, v2
	v_mov_b32_e32 v86, v2
	v_mov_b32_e32 v87, v2
	v_mov_b32_e32 v88, v2
	v_mov_b32_e32 v89, v2
	v_mov_b32_e32 v98, v2
	v_mov_b32_e32 v99, v2
	v_mov_b32_e32 v100, v2
	v_mov_b32_e32 v101, v2
	v_mov_b32_e32 v102, v2
	v_mov_b32_e32 v103, v2
	v_mov_b32_e32 v104, v2
	v_mov_b32_e32 v105, v2
	v_mov_b32_e32 v114, v2
	v_mov_b32_e32 v115, v2
	v_mov_b32_e32 v116, v2
	v_mov_b32_e32 v117, v2
	v_mov_b32_e32 v118, v2
	v_mov_b32_e32 v119, v2
	v_mov_b32_e32 v120, v2
	v_mov_b32_e32 v121, v2
	v_mov_b32_e32 v74, v2
	v_mov_b32_e32 v75, v2
	v_mov_b32_e32 v76, v2
	v_mov_b32_e32 v77, v2
	v_mov_b32_e32 v78, v2
	v_mov_b32_e32 v79, v2
	v_mov_b32_e32 v80, v2
	v_mov_b32_e32 v81, v2
	v_mov_b32_e32 v90, v2
	v_mov_b32_e32 v91, v2
	v_mov_b32_e32 v92, v2
	v_mov_b32_e32 v93, v2
	v_mov_b32_e32 v94, v2
	v_mov_b32_e32 v95, v2
	v_mov_b32_e32 v96, v2
	v_mov_b32_e32 v97, v2
	v_mov_b32_e32 v106, v2
	v_mov_b32_e32 v107, v2
	v_mov_b32_e32 v108, v2
	v_mov_b32_e32 v109, v2
	v_mov_b32_e32 v110, v2
	v_mov_b32_e32 v111, v2
	v_mov_b32_e32 v112, v2
	v_mov_b32_e32 v113, v2
	v_mov_b32_e32 v122, v2
	v_mov_b32_e32 v123, v2
	v_mov_b32_e32 v124, v2
	v_mov_b32_e32 v125, v2
	v_mov_b32_e32 v126, v2
	v_mov_b32_e32 v127, v2
	v_mov_b32_e32 v128, v2
	v_mov_b32_e32 v129, v2
	.p2align 6

.LBB0_1743:
	s_ashr_i32 s29, s28, 31
	s_lshl_b64 s[30:31], s[28:29], 21
	s_add_u32 s30, s50, s30
	s_addc_u32 s31, s51, s31
	s_and_b64 s[34:35], s[6:7], exec
	s_cselect_b32 s29, s31, s39
	s_cselect_b32 s67, s30, s38
	s_ashr_i32 s27, s26, 31
	s_lshl_b64 s[34:35], s[26:27], 21
	s_add_u32 s34, s52, s34
	s_addc_u32 s35, s53, s35
	s_and_b64 s[42:43], s[6:7], exec
	s_cselect_b32 s27, s35, s41
	s_cselect_b32 s68, s34, s40
	s_add_u32 s38, s38, 0x100080
	s_addc_u32 s39, s39, 0
	s_add_u32 s69, s40, 0x100
	v_mov_b32_e32 v2, 0
	s_addc_u32 s70, s41, 0
	s_mov_b32 s71, -2
	v_mov_b32_e32 v3, v2
	v_mov_b32_e32 v4, v2
	v_mov_b32_e32 v5, v2
	v_mov_b32_e32 v6, v2
	v_mov_b32_e32 v7, v2
	v_mov_b32_e32 v8, v2
	v_mov_b32_e32 v9, v2
	v_mov_b32_e32 v14, v2
	v_mov_b32_e32 v15, v2
	v_mov_b32_e32 v16, v2
	v_mov_b32_e32 v17, v2
	v_mov_b32_e32 v22, v2
	v_mov_b32_e32 v23, v2
	v_mov_b32_e32 v24, v2
	v_mov_b32_e32 v25, v2
	v_mov_b32_e32 v30, v2
	v_mov_b32_e32 v31, v2
	v_mov_b32_e32 v32, v2
	v_mov_b32_e32 v33, v2
	v_mov_b32_e32 v38, v2
	v_mov_b32_e32 v39, v2
	v_mov_b32_e32 v40, v2
	v_mov_b32_e32 v41, v2
	v_mov_b32_e32 v46, v2
	v_mov_b32_e32 v47, v2
	v_mov_b32_e32 v48, v2
	v_mov_b32_e32 v49, v2
	v_mov_b32_e32 v54, v2
	v_mov_b32_e32 v55, v2
	v_mov_b32_e32 v56, v2
	v_mov_b32_e32 v57, v2
	v_mov_b32_e32 v10, v2
	v_mov_b32_e32 v11, v2
	v_mov_b32_e32 v12, v2
	v_mov_b32_e32 v13, v2
	v_mov_b32_e32 v18, v2
	v_mov_b32_e32 v19, v2
	v_mov_b32_e32 v20, v2
	v_mov_b32_e32 v21, v2
	v_mov_b32_e32 v26, v2
	v_mov_b32_e32 v27, v2
	v_mov_b32_e32 v28, v2
	v_mov_b32_e32 v29, v2
	v_mov_b32_e32 v34, v2
	v_mov_b32_e32 v35, v2
	v_mov_b32_e32 v36, v2
	v_mov_b32_e32 v37, v2
	v_mov_b32_e32 v42, v2
	v_mov_b32_e32 v43, v2
	v_mov_b32_e32 v44, v2
	v_mov_b32_e32 v45, v2
	v_mov_b32_e32 v50, v2
	v_mov_b32_e32 v51, v2
	v_mov_b32_e32 v52, v2
	v_mov_b32_e32 v53, v2
	v_mov_b32_e32 v58, v2
	v_mov_b32_e32 v59, v2
	v_mov_b32_e32 v60, v2
	v_mov_b32_e32 v61, v2
	v_mov_b32_e32 v62, v2
	v_mov_b32_e32 v63, v2
	v_mov_b32_e32 v64, v2
	v_mov_b32_e32 v65, v2
	v_mov_b32_e32 v66, v2
	v_mov_b32_e32 v67, v2
	v_mov_b32_e32 v68, v2
	v_mov_b32_e32 v69, v2
	v_mov_b32_e32 v70, v2
	v_mov_b32_e32 v71, v2
	v_mov_b32_e32 v72, v2
	v_mov_b32_e32 v73, v2
	v_mov_b32_e32 v82, v2
	v_mov_b32_e32 v83, v2
	v_mov_b32_e32 v84, v2
	v_mov_b32_e32 v85, v2
	v_mov_b32_e32 v86, v2
	v_mov_b32_e32 v87, v2
	v_mov_b32_e32 v88, v2
	v_mov_b32_e32 v89, v2
	v_mov_b32_e32 v98, v2
	v_mov_b32_e32 v99, v2
	v_mov_b32_e32 v100, v2
	v_mov_b32_e32 v101, v2
	v_mov_b32_e32 v102, v2
	v_mov_b32_e32 v103, v2
	v_mov_b32_e32 v104, v2
	v_mov_b32_e32 v105, v2
	v_mov_b32_e32 v114, v2
	v_mov_b32_e32 v115, v2
	v_mov_b32_e32 v116, v2
	v_mov_b32_e32 v117, v2
	v_mov_b32_e32 v118, v2
	v_mov_b32_e32 v119, v2
	v_mov_b32_e32 v120, v2
	v_mov_b32_e32 v121, v2
	v_mov_b32_e32 v74, v2
	v_mov_b32_e32 v75, v2
	v_mov_b32_e32 v76, v2
	v_mov_b32_e32 v77, v2
	v_mov_b32_e32 v78, v2
	v_mov_b32_e32 v79, v2
	v_mov_b32_e32 v80, v2
	v_mov_b32_e32 v81, v2
	v_mov_b32_e32 v90, v2
	v_mov_b32_e32 v91, v2
	v_mov_b32_e32 v92, v2
	v_mov_b32_e32 v93, v2
	v_mov_b32_e32 v94, v2
	v_mov_b32_e32 v95, v2
	v_mov_b32_e32 v96, v2
	v_mov_b32_e32 v97, v2
	v_mov_b32_e32 v106, v2
	v_mov_b32_e32 v107, v2
	v_mov_b32_e32 v108, v2
	v_mov_b32_e32 v109, v2
	v_mov_b32_e32 v110, v2
	v_mov_b32_e32 v111, v2
	v_mov_b32_e32 v112, v2
	v_mov_b32_e32 v113, v2
	v_mov_b32_e32 v122, v2
	v_mov_b32_e32 v123, v2
	v_mov_b32_e32 v124, v2
	v_mov_b32_e32 v125, v2
	v_mov_b32_e32 v126, v2
	v_mov_b32_e32 v127, v2
	v_mov_b32_e32 v128, v2
	v_mov_b32_e32 v129, v2
	.p2align 6
